# attention tile loops: priority raised for the matrix segment and lowered for the vector segment (per-segment s_setprio pair)
# speedup vs baseline: 1.0038x; 1.0038x over previous
.LBB0_318:
	s_add_i32 s7, s4, 0xffffa000
	s_add_i32 s26, s4, 0x8000
	s_setprio 1
	s_waitcnt lgkmcnt(0)
	v_mfma_scale_f32_32x32x64_f8f6f4 v[82:97], v[178:185], v[122:129], v[2:17], v213, v213 op_sel_hi:[0,0,0]
	s_and_b32 s26, s26, 0xe000
	v_mfma_scale_f32_32x32x64_f8f6f4 v[98:113], v[194:201], v[122:129], v[2:17], v213, v213 op_sel_hi:[0,0,0]
	v_mfma_scale_f32_32x32x64_f8f6f4 v[82:97], v[186:193], v[130:137], v[82:97], v213, v213 op_sel_hi:[0,0,0]
	v_mfma_scale_f32_32x32x64_f8f6f4 v[98:113], v[170:177], v[130:137], v[98:113], v213, v213 op_sel_hi:[0,0,0]
	v_mfma_scale_f32_32x32x64_f8f6f4 v[66:81], v[162:169], v[154:161], v[66:81], v221, v220 op_sel_hi:[0,0,0] cbsz:1
	v_add_u32_e32 v158, s26, v241
	ds_read_b128 v[154:157], v158 offset:0x1800
	v_add_u32_e32 v170, s26, v240
	ds_read_b128 v[158:161], v170 offset:0x1800
	v_mfma_scale_f32_32x32x64_f8f6f4 v[50:65], v[162:169], v[146:153], v[50:65], v221, v220 op_sel_hi:[0,0,0] cbsz:1
	v_mfma_scale_f32_32x32x64_f8f6f4 v[34:49], v[162:169], v[138:145], v[34:49], v221, v220 op_sel_hi:[0,0,0] cbsz:1
	v_mfma_scale_f32_16x16x128_f8f6f4 v[202:205], v[162:169], v[114:121], v[202:205], v221, v221 op_sel_hi:[0,0,0] cbsz:1
	s_waitcnt lgkmcnt(0)
	v_mfma_scale_f32_32x32x64_f8f6f4 v[18:33], v[162:169], v[154:161], v[18:33], v221, v220 op_sel_hi:[0,0,0] cbsz:1
	s_add_i32 s26, s4, 0xffffc000
	s_and_b32 s26, s26, 0x6000
	s_setprio 0
	s_barrier
	v_add_u32_e32 v138, s26, v236
	ds_read_b128 v[178:181], v138 offset:0
	v_add_u32_e32 v139, s26, v237
	ds_read_b128 v[182:185], v139 offset:0
	ds_read_b128 v[194:197], v138 offset:0x1000
	ds_read_b128 v[198:201], v139 offset:0x1000
	v_add_u32_e32 v138, s26, v238
	ds_read_b128 v[186:189], v138 offset:0
	v_add_u32_e32 v139, s26, v239
	ds_read_b128 v[190:193], v139 offset:0
	ds_read_b128 v[170:173], v138 offset:0x1000
	ds_read_b128 v[174:177], v139 offset:0x1000
	s_and_b32 s7, s7, 0xe000
	v_add_u32_e32 v142, s7, v241
	ds_read_b128 v[154:157], v142 offset:0
	v_add_u32_e32 v162, s7, v240
	ds_read_b128 v[158:161], v162 offset:0
	ds_read_b128 v[146:149], v142 offset:0x800
	ds_read_b128 v[150:153], v162 offset:0x800
	ds_read_b128 v[138:141], v142 offset:0x1000
	ds_read_b128 v[142:145], v162 offset:0x1000
	s_add_i32 s7, s6, 4
	s_min_u32 s7, s7, s5
	s_lshl_b32 s80, s7, 14
	s_and_b32 s7, s4, 0x6000
	s_add_i32 m0, s3, s7
	s_and_b32 s7, s4, 0xe000
	v_lshl_add_u64 v[162:163], v[218:219], 0, s[80:81]
	s_add_i32 s7, s3, s7
	global_load_lds_dwordx4 v[162:163], off
	v_lshl_add_u64 v[162:163], v[162:163], 0, s[48:49]
	s_add_i32 m0, s7, 0x8000
	v_cvt_pk_u8_f32 v82, v82, 0, 0
	global_load_lds_dwordx4 v[162:163], off
	v_cvt_pk_u8_f32 v98, v98, 0, 0
	v_cvt_pk_u8_f32 v82, v83, 1, v82
	v_cvt_pk_u8_f32 v83, v99, 1, v98
	v_cvt_pk_u8_f32 v82, v84, 2, v82
	v_cvt_pk_u8_f32 v83, v100, 2, v83
	v_cvt_pk_u8_f32 v162, v85, 3, v82
	v_cvt_pk_u8_f32 v166, v101, 3, v83
	v_cvt_pk_u8_f32 v82, v86, 0, 0
	v_cvt_pk_u8_f32 v83, v102, 0, 0
	v_cvt_pk_u8_f32 v82, v87, 1, v82
	v_cvt_pk_u8_f32 v83, v103, 1, v83
	v_cvt_pk_u8_f32 v82, v88, 2, v82
	v_cvt_pk_u8_f32 v83, v104, 2, v83
	v_cvt_pk_u8_f32 v163, v89, 3, v82
	v_cvt_pk_u8_f32 v167, v105, 3, v83
	v_cvt_pk_u8_f32 v82, v90, 0, 0
	v_cvt_pk_u8_f32 v83, v106, 0, 0
	v_cvt_pk_u8_f32 v82, v91, 1, v82
	v_cvt_pk_u8_f32 v83, v107, 1, v83
	v_cvt_pk_u8_f32 v82, v92, 2, v82
	v_cvt_pk_u8_f32 v83, v108, 2, v83
	v_cvt_pk_u8_f32 v164, v93, 3, v82
	v_cvt_pk_u8_f32 v168, v109, 3, v83
	v_cvt_pk_u8_f32 v82, v94, 0, 0
	v_cvt_pk_u8_f32 v83, v110, 0, 0
	v_cvt_pk_u8_f32 v82, v95, 1, v82
	v_cvt_pk_u8_f32 v83, v111, 1, v83
	s_waitcnt vmcnt(2)
	v_cvt_pk_u8_f32 v82, v96, 2, v82
	v_cvt_pk_u8_f32 v83, v112, 2, v83
	s_addk_i32 s4, 0x2000
	s_add_i32 s6, s6, 1
	v_cvt_pk_u8_f32 v165, v97, 3, v82
	v_cvt_pk_u8_f32 v169, v113, 3, v83
	s_cmp_eq_u32 s5, s6
	s_barrier
	s_cbranch_scc0 .LBB0_318
	s_waitcnt vmcnt(0)
	s_waitcnt lgkmcnt(0)
	v_mfma_scale_f32_32x32x64_f8f6f4 v[66:81], v[162:169], v[154:161], v[66:81], v221, v220 op_sel_hi:[0,0,0] cbsz:1
	v_add_u32_e32 v2, 0x6000, v241
	ds_read_b128 v[6:9], v2 offset:0x1800
	v_add_u32_e32 v2, 0x6000, v240
	ds_read_b128 v[10:13], v2 offset:0x1800
	v_mfma_scale_f32_32x32x64_f8f6f4 v[50:65], v[162:169], v[146:153], v[50:65], v221, v220 op_sel_hi:[0,0,0] cbsz:1
	v_mfma_scale_f32_32x32x64_f8f6f4 v[34:49], v[162:169], v[138:145], v[34:49], v221, v220 op_sel_hi:[0,0,0] cbsz:1
	v_mfma_scale_f32_16x16x128_f8f6f4 v[2:5], v[162:169], v[114:121], v[202:205], v221, v221 op_sel_hi:[0,0,0] cbsz:1
	s_waitcnt lgkmcnt(0)
	v_mfma_scale_f32_32x32x64_f8f6f4 v[18:33], v[162:169], v[6:13], v[18:33], v221, v220 op_sel_hi:[0,0,0] cbsz:1
	s_and_b64 vcc, exec, s[38:39]
	s_cbranch_vccz .LBB0_321
	s_barrier

.LBB0_344:
	s_add_i32 s29, s5, 0x8000
	s_add_i32 s28, s5, 0xffffa000
	s_and_b32 s29, s29, 0xe000
	s_setprio 1
	s_waitcnt lgkmcnt(0)
	v_mfma_scale_f32_32x32x64_f8f6f4 v[82:97], v[162:169], v[122:129], v[66:81], v213, v213 op_sel_hi:[0,0,0]
	v_mfma_scale_f32_32x32x64_f8f6f4 v[98:113], v[170:177], v[122:129], v[66:81], v213, v213 op_sel_hi:[0,0,0]
	v_mfma_scale_f32_32x32x64_f8f6f4 v[50:65], v[154:161], v[146:153], v[50:65], v221, v220 op_sel_hi:[0,0,0] cbsz:1
	v_add_u32_e32 v150, s29, v192
	ds_read_b128 v[146:149], v150 offset:0x1800
	v_add_u32_e32 v162, s29, v191
	ds_read_b128 v[150:153], v162 offset:0x1800
	v_mfma_scale_f32_32x32x64_f8f6f4 v[34:49], v[154:161], v[138:145], v[34:49], v221, v220 op_sel_hi:[0,0,0] cbsz:1
	v_mfma_scale_f32_32x32x64_f8f6f4 v[18:33], v[154:161], v[130:137], v[18:33], v221, v220 op_sel_hi:[0,0,0] cbsz:1
	v_mfma_scale_f32_16x16x128_f8f6f4 v[178:181], v[154:161], v[114:121], v[178:181], v221, v221 op_sel_hi:[0,0,0] cbsz:1
	s_waitcnt lgkmcnt(0)
	v_mfma_scale_f32_32x32x64_f8f6f4 v[2:17], v[154:161], v[146:153], v[2:17], v221, v220 op_sel_hi:[0,0,0] cbsz:1
	s_add_i32 s29, s5, 0xffffc000
	s_and_b32 s29, s29, 0x6000
	s_setprio 0
	s_barrier
	v_add_u32_e32 v130, s29, v190
	ds_read_b128 v[162:165], v130 offset:0
	v_add_u32_e32 v131, s29, v193
	ds_read_b128 v[166:169], v131 offset:0
	ds_read_b128 v[170:173], v130 offset:0x1000
	ds_read_b128 v[174:177], v131 offset:0x1000
	s_and_b32 s28, s28, 0xe000
	v_add_u32_e32 v134, s28, v192
	ds_read_b128 v[146:149], v134 offset:0
	v_add_u32_e32 v154, s28, v191
	ds_read_b128 v[150:153], v154 offset:0
	ds_read_b128 v[138:141], v134 offset:0x800
	ds_read_b128 v[142:145], v154 offset:0x800
	ds_read_b128 v[130:133], v134 offset:0x1000
	ds_read_b128 v[134:137], v154 offset:0x1000
	s_add_i32 s28, s27, 4
	s_min_u32 s80, s28, s26
	s_lshl_b64 s[28:29], s[80:81], 14
	v_lshl_add_u64 v[154:155], v[184:185], 0, s[28:29]
	s_and_b32 s28, s5, 0x6000
	s_add_i32 m0, s4, s28
	s_and_b32 s28, s5, 0xe000
	s_add_i32 s28, s4, s28
	global_load_lds_dwordx4 v[154:155], off
	v_lshl_add_u64 v[154:155], v[154:155], 0, s[48:49]
	s_add_i32 m0, s28, 0x8000
	v_cvt_pk_u8_f32 v82, v82, 0, 0
	global_load_lds_dwordx4 v[154:155], off
	v_cvt_pk_u8_f32 v98, v98, 0, 0
	v_cvt_pk_u8_f32 v82, v83, 1, v82
	v_cvt_pk_u8_f32 v83, v99, 1, v98
	v_cvt_pk_u8_f32 v82, v84, 2, v82
	v_cvt_pk_u8_f32 v83, v100, 2, v83
	v_cvt_pk_u8_f32 v154, v85, 3, v82
	v_cvt_pk_u8_f32 v158, v101, 3, v83
	v_cvt_pk_u8_f32 v82, v86, 0, 0
	v_cvt_pk_u8_f32 v83, v102, 0, 0
	v_cvt_pk_u8_f32 v82, v87, 1, v82
	v_cvt_pk_u8_f32 v83, v103, 1, v83
	v_cvt_pk_u8_f32 v82, v88, 2, v82
	v_cvt_pk_u8_f32 v83, v104, 2, v83
	v_cvt_pk_u8_f32 v155, v89, 3, v82
	v_cvt_pk_u8_f32 v159, v105, 3, v83
	v_cvt_pk_u8_f32 v82, v90, 0, 0
	v_cvt_pk_u8_f32 v83, v106, 0, 0
	v_cvt_pk_u8_f32 v82, v91, 1, v82
	v_cvt_pk_u8_f32 v83, v107, 1, v83
	v_cvt_pk_u8_f32 v82, v92, 2, v82
	v_cvt_pk_u8_f32 v83, v108, 2, v83
	v_cvt_pk_u8_f32 v156, v93, 3, v82
	v_cvt_pk_u8_f32 v160, v109, 3, v83
	v_cvt_pk_u8_f32 v82, v94, 0, 0
	v_cvt_pk_u8_f32 v83, v110, 0, 0
	v_cvt_pk_u8_f32 v82, v95, 1, v82
	v_cvt_pk_u8_f32 v83, v111, 1, v83
	s_waitcnt vmcnt(2)
	v_cvt_pk_u8_f32 v82, v96, 2, v82
	v_cvt_pk_u8_f32 v83, v112, 2, v83
	s_addk_i32 s5, 0x2000
	s_add_i32 s27, s27, 1
	v_cvt_pk_u8_f32 v157, v97, 3, v82
	v_cvt_pk_u8_f32 v161, v113, 3, v83
	s_cmp_eq_u32 s26, s27
	s_barrier
	s_cbranch_scc0 .LBB0_344
	s_waitcnt vmcnt(0)
	s_lshl_b32 s4, s26, 13
	s_and_b32 s4, s4, 0xe000
	s_waitcnt lgkmcnt(0)
	v_mfma_scale_f32_32x32x64_f8f6f4 v[50:65], v[154:161], v[146:153], v[50:65], v221, v220 op_sel_hi:[0,0,0] cbsz:1
	v_add_u32_e32 v66, s4, v192
	ds_read_b128 v[70:73], v66 offset:0x1800
	v_add_u32_e32 v66, s4, v191
	ds_read_b128 v[74:77], v66 offset:0x1800
	v_mfma_scale_f32_32x32x64_f8f6f4 v[34:49], v[154:161], v[138:145], v[34:49], v221, v220 op_sel_hi:[0,0,0] cbsz:1
	v_mfma_scale_f32_32x32x64_f8f6f4 v[18:33], v[154:161], v[130:137], v[18:33], v221, v220 op_sel_hi:[0,0,0] cbsz:1
	v_mfma_scale_f32_16x16x128_f8f6f4 v[66:69], v[154:161], v[114:121], v[178:181], v221, v221 op_sel_hi:[0,0,0] cbsz:1
	s_waitcnt lgkmcnt(0)
	v_mfma_scale_f32_32x32x64_f8f6f4 v[2:17], v[154:161], v[70:77], v[2:17], v221, v220 op_sel_hi:[0,0,0] cbsz:1
	s_and_b64 vcc, exec, s[38:39]
	s_cbranch_vccz .LBB0_347
	s_barrier
